# v69 + non-temporal hint on the attention units' output stores (MLA and stick-breaking o rows)
# baseline (speedup 1.0000x reference)
; #define GAS __attribute__((address_space(1)))
; #define LAS __attribute__((address_space(3)))
; #define GAS __attribute__((address_space(1)))
; __device__ __forceinline__ float xor32(float x) { auto rr = __builtin_amdgcn_permlane32_swap(__float_as_uint(x), __float_as_uint(x), false, false); return __uint_as_float(((unsigned)(threadIdx.x & 32)) ? rr[0] : rr[1]); }
; __device__ __forceinline__ void store_o(bf16_t* orow, const f32x16& o0, const f32x16& o1, int hi, float sc, float* oss) {
;     float sq = 0.f;
; #pragma unroll
;     for (int r = 0; r < 16; ++r) sq += o0[r] * o0[r] + o1[r] * o1[r];
;     sq = (sq + xor32(sq)) * (sc * sc);
;     if (hi == 0) *(GAS float*)oss = sq;
; #pragma unroll
;     for (int half = 0; half < 2; ++half) {
;         const f32x16& o = half ? o1 : o0;
; #pragma unroll
;         for (int k = 0; k < 4; k += 2) {
;             unsigned ax = cvtpk(o[4 * k] * sc, o[4 * k + 1] * sc), ay = cvtpk(o[4 * k + 2] * sc, o[4 * k + 3] * sc);
;             unsigned bx = cvtpk(o[4 * k + 4] * sc, o[4 * k + 5] * sc), by = cvtpk(o[4 * k + 6] * sc, o[4 * k + 7] * sc);
;             { auto r = __builtin_amdgcn_permlane32_swap(ax, bx, false, false); ax = r[0]; bx = r[1]; }
;             { auto r = __builtin_amdgcn_permlane32_swap(ay, by, false, false); ay = r[0]; by = r[1]; }
;             *(GAS u32x4*)(orow + 32 * half + 8 * k + 8 * hi) = (u32x4){ax, ay, bx, by};
;         }
;     }
; }
; __device__ __forceinline__ void mla_issue(LAS unsigned char* lds, int wid, const bf16_t* ksrc, const bf16_t* rsrc, const bf16_t* vsrc, int kt) {
;     LAS unsigned char* sl_ = lds + (kt % NS) * MLA_SLOT;
;     dma16(ksrc + (size_t)kt * 64 * 512, sl_ + wid * 1024); if (wid < 4) dma16(rsrc + (size_t)kt * 64 * 32, sl_ + (8 + wid) * 1024);
;     dma16(vsrc + (size_t)kt * 64 * 512, sl_ + 12288 + wid * 1024);
; }
; __device__ __forceinline__ void mla_prologue(LAS unsigned char* lds, int tid, const bf16_t* QM, const bf16_t* KN, const bf16_t* KR, const bf16_t* VM, AU u, bf16x8 (&qr)[6]) {
;     asm volatile("" : "+v"(tid));
;     MLA_ADDR(u)
;     const bf16_t* Qw = QM + (rowb + q0 + wid * 32) * 768 + h * 96;
; #pragma unroll
;     for (int d0 = 0; d0 < 6; ++d0) qr[d0] = *(const GAS bf16x8*)(Qw + (size_t)r32 * 768 + d0 * 16 + hi * 8);
; #pragma unroll
;     for (int j = 0; j < 5; ++j) if (j < NT) mla_issue(lds, wid, ksrc, rsrc, vsrc, j);
; }
.LBB0_859:
	s_or_b64 exec, exec, s[8:9]
	v_readlane_b32 s8, v255, 36
	v_lshlrev_b64 v[4:5], 11, v[4:5]
	v_readlane_b32 s9, v255, 37
	s_lshl_b32 s88, s7, 1
	v_lshlrev_b32_e32 v0, 4, v209
	v_lshl_add_u64 v[4:5], s[8:9], 0, v[4:5]
	v_lshl_add_u64 v[4:5], v[4:5], 0, s[88:89]
	v_lshl_add_u64 v[8:9], v[4:5], 0, v[0:1]
	v_pk_mul_f32 v[4:5], v[48:49], v[2:3] op_sel_hi:[1,0]
	v_pk_mul_f32 v[6:7], v[50:51], v[2:3] op_sel_hi:[1,0]
	v_cvt_pk_bf16_f32 v4, v4, v5
	v_cvt_pk_bf16_f32 v5, v6, v7
	v_pk_mul_f32 v[6:7], v[52:53], v[2:3] op_sel_hi:[1,0]
	v_pk_mul_f32 v[10:11], v[54:55], v[2:3] op_sel_hi:[1,0]
	v_cvt_pk_bf16_f32 v6, v6, v7
	v_cvt_pk_bf16_f32 v7, v10, v11
	s_nop 0
	v_permlane32_swap_b32_e32 v4, v6
	v_permlane32_swap_b32_e32 v5, v7
	global_store_dwordx4 v[8:9], v[4:7], off offset:1024 nt
	v_pk_mul_f32 v[10:11], v[62:63], v[2:3] op_sel_hi:[1,0]
	s_add_i32 s3, s37, 1
	v_pk_mul_f32 v[4:5], v[56:57], v[2:3] op_sel_hi:[1,0]
	v_pk_mul_f32 v[6:7], v[58:59], v[2:3] op_sel_hi:[1,0]
	v_cvt_pk_bf16_f32 v4, v4, v5
	v_cvt_pk_bf16_f32 v5, v6, v7
	v_pk_mul_f32 v[6:7], v[60:61], v[2:3] op_sel_hi:[1,0]
	s_cmp_lt_i32 s3, s2
	v_cvt_pk_bf16_f32 v6, v6, v7
	v_cvt_pk_bf16_f32 v7, v10, v11
	s_nop 0
	v_permlane32_swap_b32_e32 v4, v6
	v_permlane32_swap_b32_e32 v5, v7
	global_store_dwordx4 v[8:9], v[4:7], off offset:1056 nt
	v_pk_mul_f32 v[10:11], v[22:23], v[2:3] op_sel_hi:[1,0]
	s_cselect_b64 s[8:9], -1, 0
	v_pk_mul_f32 v[4:5], v[16:17], v[2:3] op_sel_hi:[1,0]
	v_pk_mul_f32 v[6:7], v[18:19], v[2:3] op_sel_hi:[1,0]
	v_cvt_pk_bf16_f32 v4, v4, v5
	v_cvt_pk_bf16_f32 v5, v6, v7
	v_pk_mul_f32 v[6:7], v[20:21], v[2:3] op_sel_hi:[1,0]
	s_and_b64 vcc, exec, s[8:9]
	v_cvt_pk_bf16_f32 v6, v6, v7
	v_cvt_pk_bf16_f32 v7, v10, v11
	s_nop 0
	v_permlane32_swap_b32_e32 v4, v6
	v_permlane32_swap_b32_e32 v5, v7
	global_store_dwordx4 v[8:9], v[4:7], off offset:1088 nt
	s_nop 1
	v_pk_mul_f32 v[4:5], v[24:25], v[2:3] op_sel_hi:[1,0]
	v_pk_mul_f32 v[6:7], v[26:27], v[2:3] op_sel_hi:[1,0]
	v_cvt_pk_bf16_f32 v4, v4, v5
	v_cvt_pk_bf16_f32 v5, v6, v7
	v_pk_mul_f32 v[6:7], v[28:29], v[2:3] op_sel_hi:[1,0]
	v_pk_mul_f32 v[2:3], v[30:31], v[2:3] op_sel_hi:[1,0]
	v_cvt_pk_bf16_f32 v6, v6, v7
	v_cvt_pk_bf16_f32 v7, v2, v3
	s_nop 0
	v_permlane32_swap_b32_e32 v4, v6
	v_permlane32_swap_b32_e32 v5, v7
	global_store_dwordx4 v[8:9], v[4:7], off offset:1120 nt
	s_waitcnt lgkmcnt(0)
	s_barrier
	s_cbranch_vccz .LBB0_778
	s_cselect_b32 s6, s3, s37
	s_lshr_b32 s7, s6, 1
	s_mul_i32 s7, s7, s76
	s_add_i32 s7, s7, s79
	s_and_b32 s9, s7, 7
	s_ashr_i32 s8, s7, 6
	s_bfe_u32 s18, s7, 0x30003
	s_and_b32 s6, s6, 1
	s_xor_b32 s7, s9, 15
	s_cmp_eq_u32 s6, 0
	s_cselect_b32 s6, s7, s9
	v_readfirstlane_b32 s19, v189
	s_ashr_i32 s21, s19, 6
	s_ashr_i32 s9, s8, 31
	s_lshl_b64 s[8:9], s[8:9], 12
	s_lshl_b32 s7, s6, 8
	s_lshl_b32 s16, s21, 3
	s_lshl_b32 s22, s21, 5
	s_ashr_i32 s17, s16, 31
	s_and_b32 s20, s21, 3
	s_or_b32 s7, s8, s7
	s_ashr_i32 s23, s22, 31
	s_add_u32 s7, s7, s22
	s_addc_u32 s22, s9, s23
	s_mulk_i32 s22, 0x600
	s_mul_hi_u32 s23, s7, 0x600
	s_add_i32 s23, s23, s22
	s_mulk_i32 s7, 0x600
	s_add_u32 s7, s33, s7
	v_and_b32_e32 v0, 31, v189
	s_addc_u32 s23, s36, s23
	s_mul_i32 s22, s18, 0xc0
	s_add_u32 s22, s7, s22
	v_mul_u32_u24_e32 v0, 0x300, v0
	s_addc_u32 s23, s23, 0
	v_lshlrev_b32_e32 v0, 1, v0
	v_lshl_add_u64 v[2:3], s[22:23], 0, v[0:1]
	v_lshrrev_b32_e32 v0, 1, v189
	v_and_b32_e32 v0, 16, v0
	v_lshl_add_u64 v[2:3], v[2:3], 0, v[0:1]
	global_load_dwordx4 v[96:99], v[2:3], off
	global_load_dwordx4 v[100:103], v[2:3], off offset:32
	global_load_dwordx4 v[104:107], v[2:3], off offset:64
	global_load_dwordx4 v[108:111], v[2:3], off offset:96
	global_load_dwordx4 v[112:115], v[2:3], off offset:128
	global_load_dwordx4 v[116:119], v[2:3], off offset:160
	v_and_b32_e32 v0, 63, v189
	v_or_b32_e32 v2, s8, v0
	v_mov_b32_e32 v3, s9
	v_lshlrev_b64 v[4:5], 10, v[2:3]
	v_lshl_add_u64 v[4:5], s[10:11], 0, v[4:5]
	s_lshl_b32 s88, s18, 7
	v_lshl_add_u64 v[4:5], v[4:5], 0, s[88:89]
	s_lshl_b32 s88, s20, 4
	s_lshl_b32 s7, s21, 10
	s_cmp_lt_i32 s21, 4
	v_lshl_add_u64 v[4:5], s[16:17], 1, v[4:5]
	s_cselect_b64 s[16:17], -1, 0
	s_add_i32 s7, s7, 0
	v_lshlrev_b64 v[2:3], 6, v[2:3]
	s_cmp_gt_i32 s21, 3
	s_mov_b32 s21, m0
	s_mov_b32 m0, s7
	s_nop 0
	global_load_lds_dwordx4 v[4:5], off
	s_mov_b32 m0, s21
	v_lshl_add_u64 v[2:3], s[12:13], 0, v[2:3]
	v_lshl_add_u64 v[2:3], v[2:3], 0, s[88:89]
	s_cbranch_scc1 .LBB0_862
	s_add_i32 s21, s7, 0x2000
	s_mov_b32 s22, m0
	s_mov_b32 m0, s21
	s_nop 0
	global_load_lds_dwordx4 v[2:3], off
	s_mov_b32 m0, s22

; #define GAS __attribute__((address_space(1)))
; #define GAS __attribute__((address_space(1)))
; __device__ __forceinline__ float xor32(float x) { auto rr = __builtin_amdgcn_permlane32_swap(__float_as_uint(x), __float_as_uint(x), false, false); return __uint_as_float(((unsigned)(threadIdx.x & 32)) ? rr[0] : rr[1]); }
; __device__ __forceinline__ unsigned cvtpk(float lo, float hi) { f32x2 v = {lo, hi}; bf16x2_t b = __builtin_convertvector(v, bf16x2_t); return __builtin_bit_cast(unsigned, b); }
; __device__ __forceinline__ void store_o(bf16_t* orow, const f32x16& o0, const f32x16& o1, int hi, float sc, float* oss) {
;     float sq = 0.f;
; #pragma unroll
;     for (int r = 0; r < 16; ++r) sq += o0[r] * o0[r] + o1[r] * o1[r];
;     sq = (sq + xor32(sq)) * (sc * sc);
;     if (hi == 0) *(GAS float*)oss = sq;
; #pragma unroll
;     for (int half = 0; half < 2; ++half) {
;         const f32x16& o = half ? o1 : o0;
; #pragma unroll
;         for (int k = 0; k < 4; k += 2) {
;             unsigned ax = cvtpk(o[4 * k] * sc, o[4 * k + 1] * sc), ay = cvtpk(o[4 * k + 2] * sc, o[4 * k + 3] * sc);
;             unsigned bx = cvtpk(o[4 * k + 4] * sc, o[4 * k + 5] * sc), by = cvtpk(o[4 * k + 6] * sc, o[4 * k + 7] * sc);
;             { auto r = __builtin_amdgcn_permlane32_swap(ax, bx, false, false); ax = r[0]; bx = r[1]; }
;             { auto r = __builtin_amdgcn_permlane32_swap(ay, by, false, false); ay = r[0]; by = r[1]; }
;             *(GAS u32x4*)(orow + 32 * half + 8 * k + 8 * hi) = (u32x4){ax, ay, bx, by};
;         }
;     }
; }
; __device__ __forceinline__ void phase_attn(Frame& F) {
;     ...
;     for (int u = vcu; u < 1024; u += F.G) { const int bh = u >> 4; att::sb_unit(F.lds, F.tid, QKV, OA, OSS, bh >> 3, bh & 7, u & 15); }
.LBB0_875:
	s_or_b64 exec, exec, s[8:9]
	v_readlane_b32 s2, v255, 36
	v_lshlrev_b64 v[34:35], 11, v[34:35]
	v_readlane_b32 s3, v255, 37
	v_lshlrev_b32_e32 v0, 1, v114
	v_cvt_pk_bf16_f32 v18, v18, v19
	v_lshl_add_u64 v[34:35], s[2:3], 0, v[34:35]
	v_readlane_b32 s2, v255, 43
	s_lshl_b32 s88, s2, 1
	v_lshl_add_u64 v[34:35], v[34:35], 0, s[88:89]
	v_cvt_pk_bf16_f32 v19, v20, v21
	v_cvt_pk_bf16_f32 v20, v22, v23
	v_cvt_pk_bf16_f32 v21, v24, v25
	v_cvt_pk_bf16_f32 v2, v2, v3
	v_cvt_pk_bf16_f32 v3, v4, v5
	v_cvt_pk_bf16_f32 v4, v6, v7
	v_cvt_pk_bf16_f32 v5, v8, v9
	v_lshl_add_u64 v[34:35], v[34:35], 0, v[0:1]
	v_permlane32_swap_b32_e32 v18, v20
	v_permlane32_swap_b32_e32 v19, v21
	v_permlane32_swap_b32_e32 v2, v4
	v_permlane32_swap_b32_e32 v3, v5
	global_store_dwordx4 v[34:35], v[18:21], off nt
	global_store_dwordx4 v[34:35], v[2:5], off offset:64 nt
	s_nop 0
	v_cvt_pk_bf16_f32 v18, v26, v27
	v_cvt_pk_bf16_f32 v19, v28, v29
	v_cvt_pk_bf16_f32 v20, v30, v31
	v_cvt_pk_bf16_f32 v21, v32, v33
	v_cvt_pk_bf16_f32 v2, v10, v11
	v_cvt_pk_bf16_f32 v3, v12, v13
	v_cvt_pk_bf16_f32 v4, v14, v15
	v_cvt_pk_bf16_f32 v5, v16, v17
	v_permlane32_swap_b32_e32 v18, v20
	v_permlane32_swap_b32_e32 v19, v21
	v_permlane32_swap_b32_e32 v2, v4
	v_permlane32_swap_b32_e32 v3, v5
	global_store_dwordx4 v[34:35], v[18:21], off offset:32 nt
	global_store_dwordx4 v[34:35], v[2:5], off offset:96 nt
	s_waitcnt lgkmcnt(0)
	s_barrier
	s_mov_b32 s76, s101
	s_add_i32 s79, s79, s76
	s_add_i32 s78, s78, s76
	s_cmpk_lt_i32 s79, 0x400
	s_cbranch_scc0 .LBB0_892
